# scan compute loop: 24 integer RNE bf16 pair-packs (6 VALU each) fused into v_cvt_pk_bf16_f32
# speedup vs baseline: 1.0209x; 1.0209x over previous
; #define LAS __attribute__((address_space(3)))
; __device__ __forceinline__ void gdn_scan(const Params& P, LAS unsigned char* lds, int sb, int tid, int lane, int wave) {
;     ...
;         LAS unsigned char* buf = lds + par * SC_BUF;
;         bf16x8 fA[16], fB[16], fC[16], fD[8];
; #pragma unroll
;         for (int rho = 0; rho < 4; ++rho)
; #pragma unroll
;             for (int s = 0; s < 4; ++s) fA[rho * 4 + s] = *(const LAS bf16x8*)(buf + SC_WN + (16 * rho + col) * 272 + (32 * s + 8 * g) * 2);
; #pragma unroll
;         for (int rho = 0; rho < 4; ++rho)
; #pragma unroll
;             for (int s = 0; s < 4; ++s) fB[rho * 4 + s] = *(const LAS bf16x8*)(buf + SC_QD + (16 * rho + col) * 272 + (32 * s + 8 * g) * 2);
;         const LAS v4u* ufp = (const LAS v4u*)(lds + SC_UFS + par * (SCAN_NWC * 2048) + wave * 2048 + lane * 32);
;         const v4u uf0 = ufp[0], uf1 = ufp[1];
;         const float dec = ((const LAS float*)(lds + SC_DECS))[n2 & 127];
;         bf16x8 Bs[4];
; #pragma unroll
;         for (int s = 0; s < 4; ++s) Bs[s] = pack_b(S[2 * s], S[2 * s + 1]);
;         f32x4 Vn[4], Oc[4];
;         Vn[0] = (f32x4){bflo(uf0.x), bfhi(uf0.x), bflo(uf0.y), bfhi(uf0.y)}; Vn[1] = (f32x4){bflo(uf0.z), bfhi(uf0.z), bflo(uf0.w), bfhi(uf0.w)};
;         Vn[2] = (f32x4){bflo(uf1.x), bfhi(uf1.x), bflo(uf1.y), bfhi(uf1.y)}; Vn[3] = (f32x4){bflo(uf1.z), bfhi(uf1.z), bflo(uf1.w), bfhi(uf1.w)};
;         __builtin_amdgcn_sched_barrier(0);
;         PIN16(fA);
; #pragma unroll
;         for (int s = 0; s < 4; ++s)
; #pragma unroll
;             for (int rho = 0; rho < 4; ++rho) Vn[rho] = __builtin_amdgcn_mfma_f32_16x16x32_bf16(fA[rho * 4 + s], Bs[s], Vn[rho], 0, 0, 0);
;         __builtin_amdgcn_sched_barrier(0);
; #pragma unroll
;         for (int tau = 0; tau < 8; ++tau)
; #pragma unroll
;             for (int s = 0; s < 2; ++s) fC[tau * 2 + s] = *(const LAS bf16x8*)(buf + SC_KD + (16 * tau + col) * 144 + (32 * s + 8 * g) * 2);
;         __builtin_amdgcn_sched_barrier(0);
;         PIN16(fB);
; #pragma unroll
;         for (int rho = 0; rho < 4; ++rho) Oc[rho] = (f32x4){0.f, 0.f, 0.f, 0.f};
; #pragma unroll
;         for (int s = 0; s < 4; ++s)
; #pragma unroll
;             for (int rho = 0; rho < 4; ++rho) Oc[rho] = __builtin_amdgcn_mfma_f32_16x16x32_bf16(fB[rho * 4 + s], Bs[s], Oc[rho], 0, 0, 0);
.LBB0_2145:
	v_cvt_pk_bf16_f32 v56, v30, v31
	v_cvt_pk_bf16_f32 v57, v32, v33
	v_cvt_pk_bf16_f32 v58, v26, v27
	s_and_b32 s6, s1, 1
	s_mul_i32 s7, s6, 0xf400
	v_add_u32_e32 v47, s7, v46
	v_lshl_add_u32 v34, s6, 12, v1
	v_cvt_pk_bf16_f32 v59, v28, v29
	v_add_u32_e32 v158, v47, v37
	ds_read_b128 v[48:51], v34
	ds_read_b128 v[52:55], v34 offset:16
	v_mov_b32_e32 v34, s3
	v_add_u32_e32 v141, v47, v36
	ds_read_b32 v34, v34
	ds_read_b128 v[80:83], v158 offset:192
	ds_read_b128 v[84:87], v158 offset:128
	ds_read_b128 v[88:91], v158 offset:64
	ds_read_b128 v[92:95], v158
	ds_read_b128 v[96:99], v141 offset:8896
	ds_read_b128 v[100:103], v141 offset:8832
	ds_read_b128 v[104:107], v141 offset:8768
	ds_read_b128 v[108:111], v141 offset:8704
	ds_read_b128 v[112:115], v141 offset:4544
	ds_read_b128 v[116:119], v141 offset:4480
	ds_read_b128 v[120:123], v141 offset:4416
	ds_read_b128 v[124:127], v141 offset:4352
	ds_read_b128 v[128:131], v141 offset:192
	ds_read_b128 v[132:135], v141 offset:128
	ds_read_b128 v[136:139], v141 offset:64
	ds_read_b128 v[142:145], v141
	ds_read_b128 v[146:149], v158 offset:17600
	ds_read_b128 v[150:153], v158 offset:17536
	ds_read_b128 v[154:157], v158 offset:17472
	ds_read_b128 v[158:161], v158 offset:17408
	ds_read_b128 v[162:165], v141 offset:26304
	ds_read_b128 v[166:169], v141 offset:26240
	ds_read_b128 v[170:173], v141 offset:26176
	ds_read_b128 v[174:177], v141 offset:26112
	ds_read_b128 v[178:181], v141 offset:21952
	ds_read_b128 v[184:187], v141 offset:21888
	ds_read_b128 v[188:191], v141 offset:21824
	ds_read_b128 v[192:195], v141 offset:21760
	ds_read_b128 v[196:199], v141 offset:17600
	ds_read_b128 v[200:203], v141 offset:17536
	ds_read_b128 v[204:207], v141 offset:17472
	ds_read_b128 v[208:211], v141 offset:17408
	v_cvt_pk_bf16_f32 v60, v22, v23
	v_cvt_pk_bf16_f32 v61, v24, v25
	v_cvt_pk_bf16_f32 v62, v18, v19
	v_cvt_pk_bf16_f32 v63, v20, v21
	v_cvt_pk_bf16_f32 v64, v14, v15
	v_cvt_pk_bf16_f32 v65, v16, v17
	v_cvt_pk_bf16_f32 v66, v10, v11
	v_cvt_pk_bf16_f32 v67, v12, v13
	v_cvt_pk_bf16_f32 v68, v6, v7
	v_cvt_pk_bf16_f32 v69, v8, v9
	v_cvt_pk_bf16_f32 v70, v2, v3
	v_cvt_pk_bf16_f32 v71, v4, v5
	s_waitcnt lgkmcnt(0)
	v_lshlrev_b32_e32 v72, 16, v48
	v_and_b32_e32 v73, 0xffff0000, v48
	v_lshlrev_b32_e32 v74, 16, v49
	v_and_b32_e32 v75, 0xffff0000, v49
	v_lshlrev_b32_e32 v48, 16, v50
	v_and_b32_e32 v49, 0xffff0000, v50
	v_lshlrev_b32_e32 v50, 16, v51
	v_and_b32_e32 v51, 0xffff0000, v51
	v_lshlrev_b32_e32 v76, 16, v52
	v_and_b32_e32 v77, 0xffff0000, v52
	v_lshlrev_b32_e32 v78, 16, v53
	v_and_b32_e32 v79, 0xffff0000, v53
	v_lshlrev_b32_e32 v52, 16, v54
	v_and_b32_e32 v53, 0xffff0000, v54
	v_lshlrev_b32_e32 v54, 16, v55
	v_and_b32_e32 v55, 0xffff0000, v55
	s_nop 0
	v_mfma_f32_16x16x32_bf16 v[72:75], v[142:145], v[56:59], v[72:75]
	v_mfma_f32_16x16x32_bf16 v[48:51], v[124:127], v[56:59], v[48:51]
	v_mfma_f32_16x16x32_bf16 v[76:79], v[108:111], v[56:59], v[76:79]
	v_mfma_f32_16x16x32_bf16 v[52:55], v[92:95], v[56:59], v[52:55]
	v_mfma_f32_16x16x32_bf16 v[72:75], v[136:139], v[60:63], v[72:75]
	v_mfma_f32_16x16x32_bf16 v[48:51], v[120:123], v[60:63], v[48:51]
	v_mfma_f32_16x16x32_bf16 v[76:79], v[104:107], v[60:63], v[76:79]
	v_mfma_f32_16x16x32_bf16 v[52:55], v[88:91], v[60:63], v[52:55]
	v_mfma_f32_16x16x32_bf16 v[72:75], v[132:135], v[64:67], v[72:75]
	v_mfma_f32_16x16x32_bf16 v[48:51], v[116:119], v[64:67], v[48:51]
	v_mfma_f32_16x16x32_bf16 v[76:79], v[100:103], v[64:67], v[76:79]
	v_mfma_f32_16x16x32_bf16 v[52:55], v[84:87], v[64:67], v[52:55]
	v_mfma_f32_16x16x32_bf16 v[72:75], v[128:131], v[68:71], v[72:75]
	v_mfma_f32_16x16x32_bf16 v[48:51], v[112:115], v[68:71], v[48:51]
	v_mfma_f32_16x16x32_bf16 v[76:79], v[96:99], v[68:71], v[76:79]
	v_mfma_f32_16x16x32_bf16 v[52:55], v[80:83], v[68:71], v[52:55]
	v_add_u32_e32 v141, v47, v38
	v_add_u32_e32 v183, v47, v39
	v_add_u32_e32 v47, v47, v40
	ds_read_b128 v[80:83], v47 offset:34880
	ds_read_b128 v[84:87], v47 offset:34816
	ds_read_b128 v[88:91], v141 offset:48704
	ds_read_b128 v[92:95], v141 offset:48640
	ds_read_b128 v[96:99], v141 offset:46400
	ds_read_b128 v[100:103], v141 offset:46336
	ds_read_b128 v[104:107], v141 offset:44096
	ds_read_b128 v[108:111], v141 offset:44032
	ds_read_b128 v[112:115], v183 offset:34880
	ds_read_b128 v[116:119], v183 offset:34816
	ds_read_b128 v[120:123], v141 offset:39488
	ds_read_b128 v[124:127], v141 offset:39424
	ds_read_b128 v[128:131], v141 offset:37184
	ds_read_b128 v[132:135], v141 offset:37120
	ds_read_b128 v[136:139], v141 offset:34880
	ds_read_b128 v[142:145], v141 offset:34816
	s_nop 0
	v_mfma_f32_16x16x32_bf16 v[208:211], v[208:211], v[56:59], 0
	v_mfma_f32_16x16x32_bf16 v[192:195], v[192:195], v[56:59], 0
	v_mfma_f32_16x16x32_bf16 v[174:177], v[174:177], v[56:59], 0
	v_mfma_f32_16x16x32_bf16 v[56:59], v[158:161], v[56:59], 0
; #define LAS __attribute__((address_space(3)))
; #define SC_BAR() do { asm volatile("s_waitcnt lgkmcnt(0)" ::: "memory"); __builtin_amdgcn_s_barrier(); asm volatile("" ::: "memory"); } while (0)
; #define PIN8(a) asm volatile("" : "+v"(a[0]), "+v"(a[1]), "+v"(a[2]), "+v"(a[3]), "+v"(a[4]), "+v"(a[5]), "+v"(a[6]), "+v"(a[7]))
; #define PIN16(a) asm volatile("" : "+v"(a[0]), "+v"(a[1]), "+v"(a[2]), "+v"(a[3]), "+v"(a[4]), "+v"(a[5]), "+v"(a[6]), "+v"(a[7]), "+v"(a[8]), "+v"(a[9]), "+v"(a[10]), "+v"(a[11]), "+v"(a[12]), "+v"(a[13]), "+v"(a[14]), "+v"(a[15]))
; __device__ __forceinline__ void gdn_scan(const Params& P, LAS unsigned char* lds, int sb, int tid, int lane, int wave) {
;     ...
;             for (int rho = 0; rho < 4; ++rho) Oc[rho] = __builtin_amdgcn_mfma_f32_16x16x32_bf16(fB[rho * 4 + s], Bs[s], Oc[rho], 0, 0, 0);
;         __builtin_amdgcn_sched_barrier(0);
; #pragma unroll
;         for (int rho = 0; rho < 4; ++rho)
; #pragma unroll
;             for (int s = 0; s < 2; ++s) fD[rho * 2 + s] = *(const LAS bf16x8*)(buf + SC_ATT + (16 * rho + col) * 144 + (32 * s + 8 * g) * 2);
;         bf16x8 Bv[2];
;         Bv[0] = pack_b(Vn[0], Vn[1]); Bv[1] = pack_b(Vn[2], Vn[3]);
; #pragma unroll
;         for (int tau = 0; tau < 8; ++tau) S[tau] = S[tau] * dec;
;         __builtin_amdgcn_sched_barrier(0);
;         PIN16(fC);
; #pragma unroll
;         for (int s = 0; s < 2; ++s)
; #pragma unroll
;             for (int tau = 0; tau < 8; ++tau) S[tau] = __builtin_amdgcn_mfma_f32_16x16x32_bf16(fC[tau * 2 + s], Bv[s], S[tau], 0, 0, 0);
;         __builtin_amdgcn_sched_barrier(0);
;         PIN8(fD);
; #pragma unroll
;         for (int s = 0; s < 2; ++s)
; #pragma unroll
;             for (int rho = 0; rho < 4; ++rho) Oc[rho] = __builtin_amdgcn_mfma_f32_16x16x32_bf16(fD[rho * 2 + s], Bv[s], Oc[rho], 0, 0, 0);
;         LAS float* ot = (LAS float*)(lds + SC_OT + par * (64 * 36 * 4)) + 16 * wave + col;
; #pragma unroll
;         for (int rho = 0; rho < 4; ++rho)
; #pragma unroll
;             for (int i = 0; i < 4; ++i) ot[(16 * rho + 4 * g + i) * 36] = Oc[rho][i];
;         SC_BAR();
	v_mfma_f32_16x16x32_bf16 v[158:161], v[204:207], v[60:63], v[208:211]
	v_mfma_f32_16x16x32_bf16 v[188:191], v[188:191], v[60:63], v[192:195]
	v_mfma_f32_16x16x32_bf16 v[170:173], v[170:173], v[60:63], v[174:177]
	v_mfma_f32_16x16x32_bf16 v[56:59], v[154:157], v[60:63], v[56:59]
	v_mfma_f32_16x16x32_bf16 v[60:63], v[200:203], v[64:67], v[158:161]
	v_mfma_f32_16x16x32_bf16 v[154:157], v[184:187], v[64:67], v[188:191]
	v_mfma_f32_16x16x32_bf16 v[158:161], v[166:169], v[64:67], v[170:173]
	v_mfma_f32_16x16x32_bf16 v[56:59], v[150:153], v[64:67], v[56:59]
	v_mfma_f32_16x16x32_bf16 v[60:63], v[196:199], v[68:71], v[60:63]
	v_mfma_f32_16x16x32_bf16 v[64:67], v[178:181], v[68:71], v[154:157]
	v_mfma_f32_16x16x32_bf16 v[150:153], v[162:165], v[68:71], v[158:161]
	v_mfma_f32_16x16x32_bf16 v[56:59], v[146:149], v[68:71], v[56:59]
	v_cvt_pk_bf16_f32 v68, v72, v73
	v_cvt_pk_bf16_f32 v69, v74, v75
	v_cvt_pk_bf16_f32 v70, v48, v49
	v_cvt_pk_bf16_f32 v71, v50, v51
	v_cvt_pk_bf16_f32 v48, v76, v77
	v_cvt_pk_bf16_f32 v49, v78, v79
	v_cvt_pk_bf16_f32 v50, v52, v53
	v_cvt_pk_bf16_f32 v51, v54, v55
	ds_read_b128 v[52:55], v183 offset:53312
	ds_read_b128 v[72:75], v183 offset:53248
	ds_read_b128 v[76:79], v141 offset:57920
	ds_read_b128 v[146:149], v141 offset:57856
	ds_read_b128 v[154:157], v141 offset:55616
	ds_read_b128 v[158:161], v141 offset:55552
	ds_read_b128 v[162:165], v141 offset:53312
	ds_read_b128 v[166:169], v141 offset:53248
	v_pk_mul_f32 v[32:33], v[34:35], v[32:33] op_sel_hi:[0,1]
	v_pk_mul_f32 v[30:31], v[34:35], v[30:31] op_sel_hi:[0,1]
	v_pk_mul_f32 v[28:29], v[34:35], v[28:29] op_sel_hi:[0,1]
	v_pk_mul_f32 v[26:27], v[34:35], v[26:27] op_sel_hi:[0,1]
	v_pk_mul_f32 v[24:25], v[34:35], v[24:25] op_sel_hi:[0,1]
	v_pk_mul_f32 v[22:23], v[34:35], v[22:23] op_sel_hi:[0,1]
	v_pk_mul_f32 v[20:21], v[34:35], v[20:21] op_sel_hi:[0,1]
	v_pk_mul_f32 v[18:19], v[34:35], v[18:19] op_sel_hi:[0,1]
	v_pk_mul_f32 v[16:17], v[34:35], v[16:17] op_sel_hi:[0,1]
	v_pk_mul_f32 v[14:15], v[34:35], v[14:15] op_sel_hi:[0,1]
	v_pk_mul_f32 v[12:13], v[34:35], v[12:13] op_sel_hi:[0,1]
	v_pk_mul_f32 v[10:11], v[34:35], v[10:11] op_sel_hi:[0,1]
	v_pk_mul_f32 v[8:9], v[34:35], v[8:9] op_sel_hi:[0,1]
	v_pk_mul_f32 v[6:7], v[34:35], v[6:7] op_sel_hi:[0,1]
	v_pk_mul_f32 v[4:5], v[34:35], v[4:5] op_sel_hi:[0,1]
	v_pk_mul_f32 v[2:3], v[34:35], v[2:3] op_sel_hi:[0,1]
	s_waitcnt lgkmcnt(0)
	s_nop 0
	v_mfma_f32_16x16x32_bf16 v[30:33], v[142:145], v[68:71], v[30:33]
	v_mfma_f32_16x16x32_bf16 v[26:29], v[132:135], v[68:71], v[26:29]
	v_mfma_f32_16x16x32_bf16 v[22:25], v[124:127], v[68:71], v[22:25]
	v_mfma_f32_16x16x32_bf16 v[18:21], v[116:119], v[68:71], v[18:21]
	v_mfma_f32_16x16x32_bf16 v[14:17], v[108:111], v[68:71], v[14:17]
	v_mfma_f32_16x16x32_bf16 v[10:13], v[100:103], v[68:71], v[10:13]
	v_mfma_f32_16x16x32_bf16 v[6:9], v[92:95], v[68:71], v[6:9]
	v_mfma_f32_16x16x32_bf16 v[2:5], v[84:87], v[68:71], v[2:5]
	v_mfma_f32_16x16x32_bf16 v[30:33], v[136:139], v[48:51], v[30:33]
	v_mfma_f32_16x16x32_bf16 v[26:29], v[128:131], v[48:51], v[26:29]
	v_mfma_f32_16x16x32_bf16 v[22:25], v[120:123], v[48:51], v[22:25]
	v_mfma_f32_16x16x32_bf16 v[18:21], v[112:115], v[48:51], v[18:21]
	v_mfma_f32_16x16x32_bf16 v[14:17], v[104:107], v[48:51], v[14:17]
	v_mfma_f32_16x16x32_bf16 v[10:13], v[96:99], v[48:51], v[10:13]
	v_mfma_f32_16x16x32_bf16 v[6:9], v[88:91], v[48:51], v[6:9]
	v_mfma_f32_16x16x32_bf16 v[2:5], v[80:83], v[48:51], v[2:5]
	s_mulk_i32 s6, 0x2400
	v_mfma_f32_16x16x32_bf16 v[60:63], v[166:169], v[68:71], v[60:63]
	v_add_u32_e32 v34, s6, v35
	v_add_u32_e32 v47, v34, v41
	s_add_i32 s1, s1, 1
	v_mfma_f32_16x16x32_bf16 v[64:67], v[158:161], v[68:71], v[64:67]
	s_add_i32 s3, s3, 4
	s_cmpk_eq_i32 s1, 0x80
	v_mfma_f32_16x16x32_bf16 v[60:63], v[162:165], v[48:51], v[60:63]
	s_nop 7
	ds_write2_b32 v47, v60, v61 offset1:36
	ds_write_b32 v47, v62 offset:288
	v_mfma_f32_16x16x32_bf16 v[64:67], v[154:157], v[48:51], v[64:67]
	v_add_u32_e32 v60, v34, v42
	ds_write_b32 v60, v63
	v_add_u32_e32 v60, 0x800, v47
	v_mfma_f32_16x16x32_bf16 v[56:59], v[72:75], v[68:71], v[56:59]
	s_nop 3
	ds_write2_b32 v60, v64, v65 offset0:64 offset1:100
	v_mfma_f32_16x16x32_bf16 v[60:63], v[146:149], v[68:71], v[150:153]
	v_add_u32_e32 v64, v34, v43
	ds_write_b32 v47, v66 offset:2592
	ds_write_b32 v64, v67
	v_mfma_f32_16x16x32_bf16 v[60:63], v[76:79], v[48:51], v[60:63]
	v_add_u32_e32 v64, 0x1000, v47
	s_nop 6
	ds_write2_b32 v64, v60, v61 offset0:128 offset1:164
	ds_write_b32 v47, v62 offset:4896
	v_mfma_f32_16x16x32_bf16 v[48:51], v[52:55], v[48:51], v[56:59]
	v_add_u32_e32 v60, v34, v44
	ds_write_b32 v60, v63
	v_add_u32_e32 v60, 0x1800, v47
	v_add_u32_e32 v34, v34, v45
	s_nop 3
	ds_write2_b32 v60, v48, v49 offset0:192 offset1:228
	ds_write_b32 v47, v50 offset:7200
	ds_write_b32 v34, v51
	s_waitcnt lgkmcnt(0)
	s_barrier
	s_cbranch_scc0 .LBB0_2145
	s_branch .LBB0_2153
